# GLA chunk: the four LDS reads of the per-wave decay totals issued together (one wait instead of four dependent round trips)
# speedup vs baseline: 1.0066x; 1.0066x over previous
.Lgp_skip:
	v_lshlrev_b32_e32 v30, 16, v117
	v_add_f32_e32 v32, 0, v30
	v_add_u32_e32 v210, s98, v210
	global_load_ushort v178, v210, s[80:81]
	v_lshlrev_b32_e32 v30, 16, v120
	v_add_f32_e32 v40, v32, v30
	v_lshlrev_b32_e32 v30, 16, v123
	v_add_f32_e32 v41, v40, v30
	v_lshlrev_b32_e32 v30, 16, v128
	global_load_ushort v179, v210, s[80:81] offset:512
	v_add_f32_e32 v42, v41, v30
	v_lshlrev_b32_e32 v30, 16, v131
	v_add_f32_e32 v43, v42, v30
	v_lshlrev_b32_e32 v30, 16, v134
	v_add_f32_e32 v44, v43, v30
	v_add_u32_e32 v211, s99, v211
	global_load_ushort v180, v211, s[78:79]
	v_lshlrev_b32_e32 v30, 16, v137
	v_add_f32_e32 v45, v44, v30
	v_lshlrev_b32_e32 v30, 16, v140
	v_add_f32_e32 v33, v45, v30
	v_add_u32_e32 v30, s86, v91
	v_add_u32_e32 v210, s98, v210
	global_load_ushort v181, v210, s[80:81]
	ds_write_b32 v30, v33 offset:46080
	s_waitcnt lgkmcnt(0)
	s_barrier
	ds_read2st64_b32 v[30:31], v91 offset0:180 offset1:181
	ds_read2st64_b32 v[248:249], v91 offset0:182 offset1:183
	ds_read2st64_b32 v[250:251], v91 offset0:184 offset1:185
	ds_read2st64_b32 v[252:253], v91 offset0:186 offset1:187
	v_lshlrev_b32_e32 v47, 16, v115
	global_load_ushort v182, v210, s[80:81] offset:512
	v_mul_f32_e32 v47, 0x3e000000, v47
	v_lshlrev_b32_e32 v48, 16, v116
	s_andn2_b64 vcc, exec, s[18:19]
	s_waitcnt lgkmcnt(0)
	v_add_f32_e32 v30, 0, v30
	v_cndmask_b32_e64 v35, 0, v30, s[42:43]
	v_add_u32_e32 v211, s99, v211
	global_load_ushort v183, v211, s[78:79]
	v_add_f32_e32 v46, v30, v31
	v_add_f32_e32 v30, v31, v35
	v_cndmask_b32_e64 v35, v35, v30, s[44:45]
	v_add_u32_e32 v210, s98, v210
	global_load_ushort v184, v210, s[80:81]
	v_add_f32_e32 v46, v46, v248
	v_add_f32_e32 v30, v248, v35
	v_cndmask_b32_e64 v30, v35, v30, s[46:47]
	v_add_f32_e32 v35, v46, v249
	v_add_f32_e32 v31, v249, v30
	global_load_ushort v185, v210, s[80:81] offset:512
	v_cndmask_b32_e64 v46, v30, v31, s[48:49]
	v_add_f32_e32 v35, v35, v250
	v_add_f32_e32 v30, v250, v46
	v_add_u32_e32 v211, s99, v211
	global_load_ushort v186, v211, s[78:79]
	v_cndmask_b32_e64 v30, v46, v30, s[50:51]
	v_add_f32_e32 v35, v35, v251
	v_add_f32_e32 v31, v251, v30
	v_cndmask_b32_e64 v46, v30, v31, s[52:53]
	v_add_u32_e32 v210, s98, v210
	global_load_ushort v187, v210, s[80:81]
	v_add_f32_e32 v35, v35, v252
	v_add_f32_e32 v30, v252, v46
	v_cndmask_b32_e64 v30, v46, v30, s[54:55]
	v_add_f32_e32 v35, v35, v253
	v_add_f32_e32 v31, v253, v30
	global_load_ushort v188, v210, s[80:81] offset:512
	v_cndmask_b32_e64 v46, v30, v31, s[56:57]
	v_mul_f32_e32 v30, 0x3fb8aa3b, v35
	v_exp_f32_e32 v35, v30
	v_add_f32_e32 v30, v32, v46
	v_mul_f32_e32 v30, 0x3fb8aa3b, v30
	v_add_u32_e32 v211, s99, v211
	global_load_ushort v189, v211, s[78:79]
	v_exp_f32_e32 v30, v30
	v_add_f32_e32 v33, v33, v46
	v_mul_f32_e32 v33, 0x3fb8aa3b, v33
	v_exp_f32_e32 v33, v33
	v_rcp_f32_e32 v31, v30
	v_add_u32_e32 v210, s98, v210
	global_load_ushort v190, v210, s[80:81]
	v_mul_f32_e32 v30, v47, v30
	v_cvt_pk_bf16_f32 v30, v30, s0
	s_mul_i32 s0, s71, 0x480
	v_add_u32_e32 v47, s0, v92
	v_mul_f32_e32 v32, v35, v31
	global_load_ushort v192, v210, s[80:81] offset:512
	ds_write_b16 v47, v30
	v_mul_f32_e32 v30, v31, v48
	v_add_f32_e32 v31, v40, v46
	v_mul_f32_e32 v31, 0x3fb8aa3b, v31
	v_exp_f32_e32 v31, v31
	v_add_u32_e32 v211, s99, v211
	global_load_ushort v194, v211, s[78:79]
	v_cvt_pk_bf16_f32 v30, v30, s0
	ds_write_b16 v47, v30 offset:9216
	v_mul_f32_e32 v30, v32, v48
	v_rcp_f32_e32 v32, v31
	v_lshlrev_b32_e32 v40, 16, v118
	v_add_u32_e32 v210, s98, v210
	global_load_ushort v196, v210, s[80:81]
	v_mul_f32_e32 v40, 0x3e000000, v40
	v_mul_f32_e32 v31, v40, v31
	v_lshlrev_b32_e32 v48, 16, v119
	v_cvt_pk_bf16_f32 v31, v31, s0
	ds_write_b16 v47, v31 offset:144
	global_load_ushort v200, v210, s[80:81] offset:512
	v_mul_f32_e32 v31, v32, v48
	v_cvt_pk_bf16_f32 v31, v31, s0
	ds_write_b16 v47, v31 offset:9360
	v_mul_f32_e32 v31, v35, v32
	v_mul_f32_e32 v31, v31, v48
	v_add_u32_e32 v211, s99, v211
	global_load_ushort v201, v211, s[78:79]
	v_cvt_pk_bf16_f32 v31, v31, 0
	v_cvt_pk_bf16_f32 v30, v30, 0
	v_lshlrev_b32_e32 v31, 16, v31
	v_and_or_b32 v30, v30, s27, v31
	v_add_f32_e32 v31, v41, v46
	v_add_u32_e32 v210, s98, v210
	global_load_ushort v202, v210, s[80:81]
	v_mul_f32_e32 v31, 0x3fb8aa3b, v31
	v_exp_f32_e32 v31, v31
	v_lshlrev_b32_e32 v41, 16, v121
	v_mul_f32_e32 v41, 0x3e000000, v41
	v_lshlrev_b32_e32 v48, 16, v122
	global_load_ushort v203, v210, s[80:81] offset:512
	v_rcp_f32_e32 v32, v31
	v_mul_f32_e32 v31, v41, v31
	v_cvt_pk_bf16_f32 v31, v31, s0
	ds_write_b16 v47, v31 offset:288
	v_mul_f32_e32 v40, v35, v32
	v_add_u32_e32 v211, s99, v211
	global_load_ushort v206, v211, s[78:79]
	v_mul_f32_e32 v31, v32, v48
	v_add_f32_e32 v32, v42, v46
	v_mul_f32_e32 v32, 0x3fb8aa3b, v32
	v_exp_f32_e32 v32, v32
	v_cvt_pk_bf16_f32 v31, v31, s0
	v_add_u32_e32 v210, s98, v210
	global_load_ushort v207, v210, s[80:81]
	ds_write_b16 v47, v31 offset:9504
	v_mul_f32_e32 v31, v40, v48
	v_rcp_f32_e32 v40, v32
	v_lshlrev_b32_e32 v41, 16, v124
	v_mul_f32_e32 v41, 0x3e000000, v41
	global_load_ushort v208, v210, s[80:81] offset:512
	v_mul_f32_e32 v32, v41, v32
	v_lshlrev_b32_e32 v42, 16, v125
	v_cvt_pk_bf16_f32 v32, v32, s0
	ds_write_b16 v47, v32 offset:432
	v_mul_f32_e32 v32, v40, v42
	v_add_u32_e32 v211, s99, v211
	global_load_ushort v209, v211, s[78:79]
	v_cvt_pk_bf16_f32 v32, v32, s0
	ds_write_b16 v47, v32 offset:9648
	v_mul_f32_e32 v32, v35, v40
	v_mul_f32_e32 v32, v32, v42
	v_cvt_pk_bf16_f32 v32, v32, 0
	v_add_u32_e32 v214, s100, v214
	global_load_ushort v220, v214, s[80:81]
	v_cvt_pk_bf16_f32 v31, v31, 0
	v_lshlrev_b32_e32 v32, 16, v32
	v_and_or_b32 v31, v31, s27, v32
	v_add_f32_e32 v32, v43, v46
	v_mul_f32_e32 v32, 0x3fb8aa3b, v32
	v_add_u32_e32 v214, s100, v214
	global_load_ushort v219, v214, s[80:81]
	v_exp_f32_e32 v32, v32
	v_lshlrev_b32_e32 v42, 16, v129
	v_mul_f32_e32 v42, 0x3e000000, v42
	v_lshlrev_b32_e32 v43, 16, v130
	v_rcp_f32_e32 v40, v32
	v_add_u32_e32 v214, s100, v214
	global_load_ushort v222, v214, s[80:81]
	v_mul_f32_e32 v32, v42, v32
	v_cvt_pk_bf16_f32 v32, v32, s0
	ds_write_b16 v47, v32 offset:576
	v_mul_f32_e32 v41, v35, v40
	v_mul_f32_e32 v32, v40, v43
	v_add_u32_e32 v214, s100, v214
	global_load_ushort v221, v214, s[80:81]
	v_add_f32_e32 v40, v44, v46
	v_mul_f32_e32 v40, 0x3fb8aa3b, v40
	v_exp_f32_e32 v40, v40
	v_cvt_pk_bf16_f32 v32, v32, s0
	ds_write_b16 v47, v32 offset:9792
	v_add_u32_e32 v214, s100, v214
	global_load_ushort v224, v214, s[80:81]
	v_mul_f32_e32 v32, v41, v43
	v_rcp_f32_e32 v41, v40
	v_lshlrev_b32_e32 v42, 16, v132
	v_mul_f32_e32 v42, 0x3e000000, v42
	v_mul_f32_e32 v40, v42, v40
	v_add_u32_e32 v214, s100, v214
	global_load_ushort v223, v214, s[80:81]
	v_lshlrev_b32_e32 v43, 16, v133
	v_cvt_pk_bf16_f32 v40, v40, s0
	ds_write_b16 v47, v40 offset:720
	v_mul_f32_e32 v40, v41, v43
	v_cvt_pk_bf16_f32 v40, v40, s0
	ds_write_b16 v47, v40 offset:9936
	v_add_u32_e32 v214, s100, v214
	global_load_ushort v226, v214, s[80:81]
	v_mul_f32_e32 v40, v35, v41
	v_mul_f32_e32 v40, v40, v43
	v_cvt_pk_bf16_f32 v40, v40, 0
	v_cvt_pk_bf16_f32 v32, v32, 0
	v_lshlrev_b32_e32 v40, 16, v40
	v_add_u32_e32 v214, s100, v214
	global_load_ushort v225, v214, s[80:81]
	v_and_or_b32 v32, v32, s27, v40
	v_add_f32_e32 v40, v45, v46
	v_mul_f32_e32 v40, 0x3fb8aa3b, v40
	v_exp_f32_e32 v40, v40
	v_lshlrev_b32_e32 v43, 16, v135
	v_add_u32_e32 v214, s100, v214
	global_load_ushort v228, v214, s[80:81]
	v_mul_f32_e32 v43, 0x3e000000, v43
	v_lshlrev_b32_e32 v44, 16, v136
	v_rcp_f32_e32 v41, v40
	v_mul_f32_e32 v40, v43, v40
	v_cvt_pk_bf16_f32 v40, v40, s0
	v_add_u32_e32 v214, s100, v214
	global_load_ushort v227, v214, s[80:81]
	ds_write_b16 v47, v40 offset:864
	v_mul_f32_e32 v40, v41, v44
	v_mul_f32_e32 v42, v35, v41
	v_cvt_pk_bf16_f32 v40, v40, s0
	ds_write_b16 v47, v40 offset:10080
	v_add_u32_e32 v214, s100, v214
	global_load_ushort v230, v214, s[80:81]
	v_mul_f32_e32 v40, v42, v44
	v_rcp_f32_e32 v41, v33
	v_lshlrev_b32_e32 v42, 16, v138
	v_mul_f32_e32 v42, 0x3e000000, v42
	v_mul_f32_e32 v33, v42, v33
	v_add_u32_e32 v214, s100, v214
	global_load_ushort v229, v214, s[80:81]
	v_lshlrev_b32_e32 v43, 16, v139
	v_cvt_pk_bf16_f32 v33, v33, s0
	ds_write_b16 v47, v33 offset:1008
	v_mul_f32_e32 v33, v41, v43
	v_cvt_pk_bf16_f32 v33, v33, s0
	v_add_u32_e32 v214, s100, v214
	global_load_ushort v232, v214, s[80:81]
	ds_write_b16 v47, v33 offset:10224
	v_mul_f32_e32 v33, v35, v41
	v_mul_f32_e32 v33, v33, v43
	v_cvt_pk_bf16_f32 v33, v33, 0
	v_cvt_pk_bf16_f32 v40, v40, 0
	v_add_u32_e32 v214, s100, v214
	global_load_ushort v231, v214, s[80:81]
	v_lshlrev_b32_e32 v33, 16, v33
	v_and_or_b32 v33, v40, s27, v33
	v_add_u32_e32 v40, s87, v93
	ds_write_b128 v40, v[30:33] offset:18432
	s_cbranch_vccnz .LBB0_471
	ds_write_b32 v109, v35 offset:48128
